# fused GEMM epilogue: one arrival atomic per workgroup (wave 0 adds 8 after a workgroup barrier) instead of one per wave (10 sites), on top of v056
# speedup vs baseline: 1.0026x; 1.0010x over previous
.LBB0_612:
	s_or_b64 exec, exec, s[8:9]
	s_lshl_b32 s4, s83, 6
	s_ashr_i32 s5, s4, 31
	s_lshl_b64 s[4:5], s[4:5], 2
	s_add_u32 s4, s28, s4
	s_addc_u32 s5, s29, s5
	s_waitcnt vmcnt(0)
	s_barrier
	s_add_u32 s28, s4, 0x10000
	s_addc_u32 s29, s5, 0
	v_cmp_ne_u32_e64 s[48:49], 0, v0
	v_cmp_eq_u32_e64 s[46:47], 0, v0
	s_and_saveexec_b64 s[8:9], s[46:47]
	s_cbranch_execz .LBB0_615
	s_mov_b64 s[30:31], exec
	v_mbcnt_lo_u32_b32 v0, s30, 0
	v_mbcnt_hi_u32_b32 v0, s31, v0
	v_cmp_eq_u32_e32 vcc, 0, v0
	s_and_b64 s[4:5], exec, vcc
	s_mov_b64 exec, s[4:5]
	s_cbranch_execz .LBB0_615
	s_cmp_gt_u32 s80, 63
	s_cbranch_scc1 .LBB0_615
	s_bcnt1_i32_b64 s4, s[30:31]
	s_lshl_b32 s4, s4, 3
	v_mov_b32_e32 v0, s4
	global_atomic_add v1, v0, s[28:29]

.LBB0_710:
	s_or_b64 exec, exec, s[8:9]
	s_lshl_b32 s4, s4, 6
	s_ashr_i32 s5, s4, 31
	s_lshl_b64 s[4:5], s[4:5], 2
	s_add_u32 s4, s26, s4
	s_addc_u32 s5, s27, s5
	s_waitcnt vmcnt(0)
	s_barrier
	s_add_u32 s26, s4, 0x10000
	s_addc_u32 s27, s5, 0
	v_cmp_ne_u32_e64 s[46:47], 0, v0
	v_cmp_eq_u32_e64 s[44:45], 0, v0
	s_and_saveexec_b64 s[8:9], s[44:45]
	s_cbranch_execz .LBB0_713
	s_mov_b64 s[28:29], exec
	v_mbcnt_lo_u32_b32 v0, s28, 0
	v_mbcnt_hi_u32_b32 v0, s29, v0
	v_cmp_eq_u32_e32 vcc, 0, v0
	s_and_b64 s[4:5], exec, vcc
	s_mov_b64 exec, s[4:5]
	s_cbranch_execz .LBB0_713
	s_cmp_gt_u32 s70, 63
	s_cbranch_scc1 .LBB0_713
	s_bcnt1_i32_b64 s4, s[28:29]
	s_lshl_b32 s4, s4, 3
	v_mov_b32_e32 v0, s4
	global_atomic_add v1, v0, s[26:27]

.LBB0_1551:
	s_or_b64 exec, exec, s[8:9]
	s_lshl_b32 s8, s47, 6
	s_ashr_i32 s9, s8, 31
	s_lshl_b64 s[8:9], s[8:9], 2
	s_add_u32 s4, s22, s8
	s_addc_u32 s8, s23, s9
	s_waitcnt vmcnt(0)
	s_barrier
	s_add_u32 s22, s4, 0x10000
	s_addc_u32 s23, s8, 0
	v_cmp_ne_u32_e64 s[46:47], 0, v0
	v_cmp_eq_u32_e64 s[44:45], 0, v0
	s_and_saveexec_b64 s[8:9], s[44:45]
	s_cbranch_execz .LBB0_1554
	s_mov_b64 s[24:25], exec
	v_mbcnt_lo_u32_b32 v0, s24, 0
	v_mbcnt_hi_u32_b32 v0, s25, v0
	v_cmp_eq_u32_e32 vcc, 0, v0
	s_and_b64 s[26:27], exec, vcc
	s_mov_b64 exec, s[26:27]
	s_cbranch_execz .LBB0_1554
	s_cmp_gt_u32 s48, 63
	s_cbranch_scc1 .LBB0_1554
	s_bcnt1_i32_b64 s4, s[24:25]
	s_lshl_b32 s4, s4, 3
	v_mov_b32_e32 v0, s4
	global_atomic_add v1, v0, s[22:23]

.LBB0_1648:
	s_or_b64 exec, exec, s[8:9]
	s_lshl_b32 s8, s4, 6
	s_ashr_i32 s9, s8, 31
	s_lshl_b64 s[8:9], s[8:9], 2
	s_add_u32 s4, s22, s8
	s_addc_u32 s8, s23, s9
	s_waitcnt vmcnt(0)
	s_barrier
	s_add_u32 s22, s4, 0x10000
	s_addc_u32 s23, s8, 0
	v_cmp_ne_u32_e64 s[44:45], 0, v0
	v_cmp_eq_u32_e64 s[42:43], 0, v0
	s_and_saveexec_b64 s[8:9], s[42:43]
	s_cbranch_execz .LBB0_1651
	s_mov_b64 s[24:25], exec
	v_mbcnt_lo_u32_b32 v0, s24, 0
	v_mbcnt_hi_u32_b32 v0, s25, v0
	v_cmp_eq_u32_e32 vcc, 0, v0
	s_and_b64 s[26:27], exec, vcc
	s_mov_b64 exec, s[26:27]
	s_cbranch_execz .LBB0_1651
	s_cmp_gt_u32 s46, 63
	s_cbranch_scc1 .LBB0_1651
	s_bcnt1_i32_b64 s4, s[24:25]
	s_lshl_b32 s4, s4, 3
	v_mov_b32_e32 v0, s4
	global_atomic_add v1, v0, s[22:23]

.LBB0_2393:
	s_or_b64 exec, exec, s[26:27]
	s_lshl_b32 s10, s94, 6
	s_ashr_i32 s11, s10, 31
	s_lshl_b64 s[10:11], s[10:11], 2
	s_add_u32 s4, s24, s10
	s_addc_u32 s8, s25, s11
	s_waitcnt vmcnt(0)
	s_barrier
	s_add_u32 s24, s4, 0x10000
	s_addc_u32 s25, s8, 0
	v_cmp_ne_u32_e64 s[46:47], 0, v167
	v_cmp_eq_u32_e64 s[44:45], 0, v167
	s_and_saveexec_b64 s[26:27], s[44:45]
	s_cbranch_execz .LBB0_2396
	s_mov_b64 s[28:29], exec
	v_mbcnt_lo_u32_b32 v166, s28, 0
	v_mbcnt_hi_u32_b32 v166, s29, v166
	v_cmp_eq_u32_e32 vcc, 0, v166
	s_and_b64 s[10:11], exec, vcc
	s_mov_b64 exec, s[10:11]
	s_cbranch_execz .LBB0_2396
	s_cmp_gt_u32 s83, 63
	s_cbranch_scc1 .LBB0_2396
	s_bcnt1_i32_b64 s4, s[28:29]
	s_lshl_b32 s4, s4, 3
	v_mov_b32_e32 v166, s4
	global_atomic_add v1, v166, s[24:25]

.LBB0_2493:
	s_or_b64 exec, exec, s[24:25]
	s_lshl_b32 s10, s4, 6
	s_ashr_i32 s11, s10, 31
	s_lshl_b64 s[10:11], s[10:11], 2
	s_add_u32 s4, s22, s10
	s_addc_u32 s8, s23, s11
	s_waitcnt vmcnt(0)
	s_barrier
	s_add_u32 s22, s4, 0x10000
	s_addc_u32 s23, s8, 0
	v_cmp_ne_u32_e64 s[44:45], 0, v166
	v_cmp_eq_u32_e64 s[42:43], 0, v166
	s_and_saveexec_b64 s[24:25], s[42:43]
	s_cbranch_execz .LBB0_2496
	s_mov_b64 s[26:27], exec
	v_mbcnt_lo_u32_b32 v166, s26, 0
	v_mbcnt_hi_u32_b32 v166, s27, v166
	v_cmp_eq_u32_e32 vcc, 0, v166
	s_and_b64 s[10:11], exec, vcc
	s_mov_b64 exec, s[10:11]
	s_cbranch_execz .LBB0_2496
	s_cmp_gt_u32 s78, 63
	s_cbranch_scc1 .LBB0_2496
	s_bcnt1_i32_b64 s4, s[26:27]
	s_lshl_b32 s4, s4, 3
	v_mov_b32_e32 v166, s4
	global_atomic_add v1, v166, s[22:23]

.LBB0_2728:
	s_or_b64 exec, exec, s[22:23]
	s_lshl_b32 s22, s53, 6
	s_ashr_i32 s23, s22, 31
	s_lshl_b64 s[22:23], s[22:23], 2
	s_add_u32 s4, s18, s22
	s_addc_u32 s13, s19, s23
	s_waitcnt vmcnt(0)
	s_barrier
	s_add_u32 s18, s4, 0x10000
	s_addc_u32 s19, s13, 0
	v_cmp_ne_u32_e64 s[46:47], 0, v167
	v_cmp_eq_u32_e64 s[44:45], 0, v167
	s_and_saveexec_b64 s[22:23], s[44:45]
	s_cbranch_execz .LBB0_2731
	s_mov_b64 s[24:25], exec
	v_mbcnt_lo_u32_b32 v166, s24, 0
	v_mbcnt_hi_u32_b32 v166, s25, v166
	v_cmp_eq_u32_e32 vcc, 0, v166
	s_and_b64 s[26:27], exec, vcc
	s_mov_b64 exec, s[26:27]
	s_cbranch_execz .LBB0_2731
	s_cmp_gt_u32 s49, 63
	s_cbranch_scc1 .LBB0_2731
	s_bcnt1_i32_b64 s4, s[24:25]
	s_lshl_b32 s4, s4, 3
	v_mov_b32_e32 v166, s4
	global_atomic_add v1, v166, s[18:19]

.LBB0_2821:
	s_or_b64 exec, exec, s[22:23]
	s_lshl_b32 s22, s4, 6
	s_ashr_i32 s23, s22, 31
	s_lshl_b64 s[22:23], s[22:23], 2
	s_add_u32 s4, s18, s22
	s_addc_u32 s13, s19, s23
	s_waitcnt vmcnt(0)
	s_barrier
	s_add_u32 s18, s4, 0x10000
	s_addc_u32 s19, s13, 0
	v_cmp_ne_u32_e64 s[46:47], 0, v167
	v_cmp_eq_u32_e64 s[44:45], 0, v167
	s_and_saveexec_b64 s[22:23], s[44:45]
	s_cbranch_execz .LBB0_2824
	s_mov_b64 s[24:25], exec
	v_mbcnt_lo_u32_b32 v166, s24, 0
	v_mbcnt_hi_u32_b32 v166, s25, v166
	v_cmp_eq_u32_e32 vcc, 0, v166
	s_and_b64 s[26:27], exec, vcc
	s_mov_b64 exec, s[26:27]
	s_cbranch_execz .LBB0_2824
	s_cmp_gt_u32 s49, 63
	s_cbranch_scc1 .LBB0_2824
	s_bcnt1_i32_b64 s4, s[24:25]
	s_lshl_b32 s4, s4, 3
	v_mov_b32_e32 v166, s4
	global_atomic_add v1, v166, s[18:19]

.LBB0_2916:
	s_or_b64 exec, exec, s[22:23]
	s_lshl_b32 s20, s52, 6
	s_ashr_i32 s21, s20, 31
	s_lshl_b64 s[20:21], s[20:21], 2
	s_add_u32 s4, s16, s20
	s_addc_u32 s17, s17, s21
	s_waitcnt vmcnt(0)
	s_barrier
	s_add_u32 s16, s4, 0x10000
	s_addc_u32 s17, s17, 0
	v_cmp_ne_u32_e64 s[46:47], 0, v168
	v_cmp_eq_u32_e64 s[44:45], 0, v168
	s_and_saveexec_b64 s[20:21], s[44:45]
	s_cbranch_execz .LBB0_2919
	s_mov_b64 s[22:23], exec
	v_mbcnt_lo_u32_b32 v168, s22, 0
	v_mbcnt_hi_u32_b32 v168, s23, v168
	v_cmp_eq_u32_e32 vcc, 0, v168
	s_and_b64 s[24:25], exec, vcc
	s_mov_b64 exec, s[24:25]
	s_cbranch_execz .LBB0_2919
	s_cmp_gt_u32 s48, 63
	s_cbranch_scc1 .LBB0_2919
	s_bcnt1_i32_b64 s4, s[22:23]
	s_lshl_b32 s4, s4, 3
	v_mov_b32_e32 v168, s4
	global_atomic_add v1, v168, s[16:17]

.LBB0_3007:
	s_or_b64 exec, exec, s[22:23]
	s_lshl_b32 s20, s4, 6
	s_ashr_i32 s21, s20, 31
	s_lshl_b64 s[20:21], s[20:21], 2
	s_add_u32 s4, s16, s20
	s_addc_u32 s17, s17, s21
	s_waitcnt vmcnt(0)
	s_barrier
	s_add_u32 s16, s4, 0x10000
	s_addc_u32 s17, s17, 0
	v_cmp_ne_u32_e64 s[44:45], 0, v168
	v_cmp_eq_u32_e64 s[42:43], 0, v168
	s_and_saveexec_b64 s[20:21], s[42:43]
	s_cbranch_execz .LBB0_3010
	s_mov_b64 s[22:23], exec
	v_mbcnt_lo_u32_b32 v168, s22, 0
	v_mbcnt_hi_u32_b32 v168, s23, v168
	v_cmp_eq_u32_e32 vcc, 0, v168
	s_and_b64 s[24:25], exec, vcc
	s_mov_b64 exec, s[24:25]
	s_cbranch_execz .LBB0_3010
	s_cmp_gt_u32 s46, 63
	s_cbranch_scc1 .LBB0_3010
	s_bcnt1_i32_b64 s4, s[22:23]
	s_lshl_b32 s4, s4, 3
	v_mov_b32_e32 v168, s4
	global_atomic_add v1, v168, s[16:17]
